# prologue: the x->bf16 rows are shared by all 2048 waves (the early-finishing strip waves take their share) instead of by the 1152 non-strip waves
# speedup vs baseline: 1.0078x; 1.0078x over previous
; template <int I> __device__ __forceinline__ const float* karg_in() { return (const float*)(const GAS float*)karg_u64<I>(); }
; __device__ __forceinline__ unsigned char* karg_ws() { return (unsigned char*)(GAS unsigned char*)karg_u64<15>(); }
; __device__ __forceinline__ void p0_prologue(const Frame& F) {
;     ...
;     const int gw = F.vcu * 8 + F.wave, NGW = F.G * 8;
;     unsigned char* ws = karg_ws();
;     constexpr int I_POOL = (512 / 64) * (D / 32);
;     constexpr int I_EOUT = (512 / 64) * (D / 32), I_EIN = (D / 64) * (EIN / 32), I_OQKV = (D / 64) * (3 * D / 32), I_OOUT = (D / 64) * (D / 32), I_UP = (D / 64) * (2 * FF / 32), I_DN = (FF / 64) * (D / 32);
;     constexpr int NITEMS = 2 * (I_EOUT + I_EIN + I_OOUT) + 4 * I_DN;
;     const int role = gw & 3, ridx = gw >> 2;
;     constexpr int NSTR = 4 * N_STRIPS + 2 * Q_STRIPS;
;     if (role == 0 && ridx < 2 * I_POOL) { const int it = ridx; const int l = it / I_POOL, r = it % I_POOL; const int nblk = D / 32, kb = r / nblk, nb = r % nblk;
;         pool_item(karg_in<4>() + (size_t)l * D * D, karg_in<7>() + (size_t)l * 4 * 128 * 128, karg_in<8>() + (size_t)l * 512, (bf16_t*)(ws + WS_W_EOUT + l * SZ_SQ), 512 + 64 * kb, 32 * nb, scr, F.lane); }
;     else if (role == 1 || (role == 2 && ridx < NSTR - 512)) { const int sidx = role == 1 ? ridx : 512 + ridx;
;         if (sidx < 4 * N_STRIPS) up_strip(sidx / N_STRIPS, sidx % N_STRIPS, ws, scr, F.lane); else { const int q = sidx - 4 * N_STRIPS; qkv_strip(q / Q_STRIPS, q % Q_STRIPS, ws, scr, F.lane); } }
.LBB0_10:
	s_lshl_b32 s1, s78, 14
	s_add_i32 s3, s1, 0
	s_bfe_u32 s1, s0, 0x20006
	s_cmp_lg_u32 s1, 0
	s_cselect_b64 s[18:19], -1, 0
	s_cmp_eq_u32 s1, 0
	s_cselect_b64 s[8:9], -1, 0
	s_cmp_eq_u32 s1, 1
	s_cselect_b64 s[22:23], -1, 0
	s_cmp_eq_u32 s1, 2
	s_cselect_b64 s[24:25], -1, 0
	s_cmp_eq_u32 s1, 3
	s_cselect_b64 s[4:5], -1, 0
	s_cmp_lg_u32 s1, 3
	s_cselect_b64 s[20:21], -1, 0
	s_lshl_b32 s6, s6, 3
	s_add_i32 s6, s6, s78
	s_mov_b32 s100, s6
	s_ashr_i32 s16, s6, 2
	s_cmpk_lt_i32 s16, 0x200
	s_load_dwordx2 s[14:15], s[76:77], 0x78
	s_waitcnt lgkmcnt(0)
	s_cselect_b64 s[6:7], -1, 0
	s_and_b64 s[6:7], s[8:9], s[6:7]
	v_and_b32_e32 v68, 63, v69
	s_andn2_b64 vcc, exec, s[6:7]
	s_mov_b64 s[6:7], -1
	s_cbranch_vccz .LBB0_141
	s_cmpk_lt_i32 s16, 0x180
	s_cselect_b64 s[6:7], -1, 0
	s_and_b64 s[6:7], s[24:25], s[6:7]
	s_or_b64 s[6:7], s[22:23], s[6:7]
	s_andn2_b64 vcc, exec, s[6:7]
	s_mov_b64 s[6:7], -1
	s_cbranch_vccz .LBB0_124
	s_andn2_b64 vcc, exec, s[18:19]
	s_cbranch_vccnz .LBB0_123
	s_add_i32 s6, s16, 0x80
	s_and_b64 s[4:5], s[4:5], exec
	s_cselect_b32 s5, s16, s6
	s_cmpk_lt_i32 s5, 0x2300
	s_cselect_b64 s[10:11], -1, 0
	s_cmpk_gt_i32 s5, 0x22ff
	s_cbranch_scc1 .LBB0_18
	s_cmpk_gt_i32 s5, 0x1ff
	s_cbranch_scc0 .LBB0_19
	s_cmpk_gt_u32 s5, 0x8ff
	s_mov_b64 s[28:29], -1
	s_cbranch_scc0 .LBB0_20
	s_cmpk_gt_u32 s5, 0xcff
	s_cbranch_scc0 .LBB0_21
	s_add_i32 s4, s5, 0xf300
	s_and_b32 s6, s4, 0xffff
	s_mul_i32 s6, s6, 0xba2f
	s_lshr_b32 s8, s6, 26
	s_mul_i32 s6, s8, 0x580
	s_sub_i32 s4, s4, s6
	s_and_b32 s6, s4, 0xffff
	s_lshl_b32 s4, s6, 1
	s_lshl_b32 s6, s6, 5
	s_and_b32 s4, s4, 0xfc0
	s_and_b32 s17, s6, 0x3e0
	s_mul_i32 s9, s8, 0xb00000
	s_load_dwordx2 s[6:7], s[76:77], 0x68
	s_waitcnt lgkmcnt(0)
	s_add_u32 s12, s6, s9
	s_addc_u32 s13, s7, 0
	s_mul_i32 s8, s8, 0x580000
	s_add_u32 s6, s14, s8
	s_addc_u32 s7, s15, 0
	s_add_u32 s6, s6, 0x4800000
	s_addc_u32 s7, s7, 0
	s_mov_b64 s[8:9], 0
	s_branch .LBB0_22

; #define GAS __attribute__((address_space(1)))
; __device__ __forceinline__ unsigned pk2(float lo, float hi) { return f2bf(lo) | (f2bf(hi) << 16); }
; __device__ __forceinline__ void p0_prologue(const Frame& F) {
;     ...
;     const bool is_strip = (role == 1) || (role == 2 && ridx < NSTR - 512);
;     if (!is_strip) {
;         const int NRW = NGW - NSTR;
;         const int rw = role == 0 ? ridx : (role == 3 ? 512 + ridx : 1024 + ridx - (NSTR - 512));
;         for (int m = rw; m < M; m += 2 * NRW) {
;             const int m2 = m + NRW; const bool two = m2 < M;
;             const GAS f32x4* xr = (const GAS f32x4*)(x + (size_t)m * D) + F.lane; const GAS f32x4* xr2 = (const GAS f32x4*)(x + (size_t)(two ? m2 : m) * D) + F.lane; f32x4 v[4], v2[4]; float s = 0.f, s2 = 0.f;
; #pragma unroll
;             for (int j = 0; j < 4; ++j) { v[j] = __builtin_nontemporal_load(&xr[64 * j]); v2[j] = __builtin_nontemporal_load(&xr2[64 * j]); }
; #pragma unroll
;             for (int j = 0; j < 4; ++j) { s += (v[j][0] * v[j][0] + v[j][1] * v[j][1]) + (v[j][2] * v[j][2] + v[j][3] * v[j][3]); s2 += (v2[j][0] * v2[j][0] + v2[j][1] * v2[j][1]) + (v2[j][2] * v2[j][2] + v2[j][3] * v2[j][3]); }
;             s = wave_sum(s); s2 = wave_sum(s2);
;             GAS unsigned long long* o8 = (GAS unsigned long long*)(xb + (size_t)m * D) + F.lane;
; #pragma unroll
;             for (int j = 0; j < 4; ++j) o8[64 * j] = (unsigned long long)pk2(v[j][0], v[j][1]) | ((unsigned long long)pk2(v[j][2], v[j][3]) << 32);
;             if (F.lane < 16) ssp[(size_t)m * 16 + F.lane] = (F.lane == 0) ? s : 0.f;
;             if (two) { GAS unsigned long long* o82 = (GAS unsigned long long*)(xb + (size_t)m2 * D) + F.lane;
.LBB0_145:
	s_cmpk_lt_i32 s16, 0x180
	s_cselect_b64 s[4:5], -1, 0
	s_load_dwordx2 s[26:27], s[76:77], 0
	s_waitcnt lgkmcnt(0)
	s_mov_b32 s16, s100
.LBB0_149:
.LBB0_150:
.LBB0_151:
.LBB0_152:
	s_cmpk_gt_i32 s16, 0x3fff
	s_cbranch_scc1 .LBB0_161
	s_waitcnt vmcnt(15)
	v_mbcnt_lo_u32_b32 v2, -1, 0
	v_mbcnt_hi_u32_b32 v2, -1, v2
	v_and_b32_e32 v3, 64, v2
	v_add_u32_e32 v3, 64, v3
	s_waitcnt vmcnt(13)
	v_xor_b32_e32 v4, 1, v2
	v_cmp_lt_i32_e32 vcc, v4, v3
	v_mov_b32_e32 v1, 0
	s_lshl_b32 s2, s2, 3
	v_cndmask_b32_e32 v4, v2, v4, vcc
	v_lshlrev_b32_e32 v32, 2, v4
	v_xor_b32_e32 v4, 2, v2
	v_cmp_lt_i32_e32 vcc, v4, v3
	s_mov_b64 s[4:5], 0x5e00000
	v_cndmask_b32_e32 v4, v2, v4, vcc
	v_lshlrev_b32_e32 v33, 2, v4
	v_xor_b32_e32 v4, 4, v2
	v_cmp_lt_i32_e32 vcc, v4, v3
	s_ashr_i32 s17, s16, 31
	s_lshl_b32 s8, s2, 1
	v_cndmask_b32_e32 v4, v2, v4, vcc
	v_lshlrev_b32_e32 v34, 2, v4
	v_xor_b32_e32 v4, 8, v2
	v_cmp_lt_i32_e32 vcc, v4, v3
	s_lshl_b64 s[12:13], s[16:17], 6
	s_mov_b64 s[10:11], 0x7e00000
	v_cndmask_b32_e32 v4, v2, v4, vcc
	v_lshlrev_b32_e32 v35, 2, v4
	v_xor_b32_e32 v4, 16, v2
	v_cmp_lt_i32_e32 vcc, v4, v3
	s_ashr_i32 s9, s8, 31
	s_lshl_b64 s[18:19], s[16:17], 12
	v_cndmask_b32_e32 v4, v2, v4, vcc
	v_lshlrev_b32_e32 v36, 2, v4
	v_xor_b32_e32 v4, 32, v2
	v_cmp_lt_i32_e32 vcc, v4, v3
	v_mov_b32_e32 v3, v1
	v_lshlrev_b32_e32 v0, 4, v68
	v_cndmask_b32_e32 v2, v2, v4, vcc
	v_lshlrev_b32_e32 v37, 2, v2
	v_lshlrev_b32_e32 v2, 3, v68
	v_lshl_add_u64 v[4:5], s[14:15], 0, v[2:3]
	s_waitcnt vmcnt(9)
	v_lshl_add_u64 v[22:23], v[4:5], 0, s[4:5]
	v_lshlrev_b32_e32 v4, 2, v68
	v_mov_b32_e32 v5, v1
	v_lshl_add_u64 v[6:7], s[14:15], 0, v[4:5]
	v_lshl_add_u64 v[4:5], s[12:13], 0, v[4:5]
	s_lshl_b64 s[12:13], s[16:17], 11
	v_lshl_add_u64 v[24:25], v[6:7], 0, s[10:11]
	v_lshl_add_u64 v[26:27], v[4:5], 0, s[10:11]
	s_lshl_b64 s[10:11], s[8:9], 6
	s_waitcnt vmcnt(8)
	v_or_b32_e32 v28, s12, v2
	v_mov_b32_e32 v29, s13
	s_lshl_b64 s[12:13], s[8:9], 11
	s_add_u32 s18, s26, s18
	s_addc_u32 s19, s27, s19
	v_lshl_add_u64 v[20:21], s[26:27], 0, v[0:1]
	v_lshl_add_u64 v[0:1], s[18:19], 0, v[0:1]
	s_mov_b64 s[18:19], 0x800
	v_cmp_gt_u32_e64 s[4:5], 16, v68
	v_cmp_eq_u32_e64 s[6:7], 0, v68
	v_lshl_add_u64 v[30:31], v[0:1], 0, s[18:19]
	s_lshl_b64 s[18:19], s[8:9], 12
	s_movk_i32 s3, 0x7fff
	s_mov_b32 s9, 0xffff0000
	s_mov_b32 s17, 0x5e00000
	s_branch .LBB0_156
